# speedup vs baseline: 1.0150x; 1.0150x over previous
_Z13stage0_kernel5TJobs6S0Args:
	s_mov_b32 s3, 0xa1e
	s_cmpk_lt_u32 s2, 0x409
	s_cselect_b32 s3, s3, 0xfffffbf7
	s_add_i32 s2, s2, s3
	s_load_dwordx16 s[4:19], s[0:1], 0x120
	s_load_dwordx16 s[36:51], s[0:1], 0x1e0
	s_add_u32 s34, s0, 0x120
	s_addc_u32 s35, s1, 0
	s_cmpk_gt_i32 s2, 0xcb
	s_waitcnt lgkmcnt(0)
	v_writelane_b32 v83, s4, 0
	s_nop 1
	v_writelane_b32 v83, s5, 1
	v_writelane_b32 v83, s6, 2
	v_writelane_b32 v83, s7, 3
	v_writelane_b32 v83, s8, 4
	v_writelane_b32 v83, s9, 5
	v_writelane_b32 v83, s10, 6
	v_writelane_b32 v83, s11, 7
	v_writelane_b32 v83, s12, 8
	v_writelane_b32 v83, s13, 9
	v_writelane_b32 v83, s14, 10
	v_writelane_b32 v83, s15, 11
	v_writelane_b32 v83, s16, 12
	v_writelane_b32 v83, s17, 13
	v_writelane_b32 v83, s18, 14
	v_writelane_b32 v83, s19, 15
	s_mov_b64 s[4:5], -1
	s_cbranch_scc0 .LBB0_116
	s_load_dword s4, s[34:35], 0x114
	s_add_i32 s3, s2, 0xffffff34
	v_writelane_b32 v83, s3, 16
	s_waitcnt lgkmcnt(0)
	s_cmp_ge_i32 s3, s4
	s_mov_b32 s3, s4
	s_mov_b64 s[4:5], -1
	s_cbranch_scc0 .LBB0_93
	s_mov_b32 s4, s3
	s_load_dword s3, s[0:1], 0x230
	s_waitcnt lgkmcnt(0)
	s_add_i32 s3, s3, s4
	v_readlane_b32 s4, v83, 16
	s_cmp_ge_i32 s4, s3
	s_mov_b64 s[4:5], -1
	s_cbranch_scc0 .LBB0_80
	s_sub_i32 s4, s2, 0xcc
	s_sub_i32 s4, s4, s3
	s_load_dwordx2 s[8:9], s[0:1], 0x198
	s_load_dwordx16 s[12:27], s[0:1], 0x1a0
	s_load_dwordx4 s[28:31], s[0:1], 0x1e0
	v_lshlrev_b32_e32 v5, 5, v0
	v_and_b32_e32 v6, 0x7f, v0
	v_lshlrev_b32_e32 v6, 4, v6
	s_waitcnt lgkmcnt(0)
	global_load_dwordx4 v[8:11], v5, s[16:17]
	global_load_dwordx4 v[12:15], v5, s[16:17] offset:16
	global_load_dwordx4 v[16:19], v6, s[26:27]
	s_waitcnt vmcnt(0)
	ds_write_b128 v5, v[8:11]
	ds_write_b128 v5, v[12:15] offset:16
	ds_write_b128 v6, v[16:19] offset:8192
	s_waitcnt lgkmcnt(0)
	s_barrier
	v_lshrrev_b32_e32 v1, 7, v0
	s_nop 0
	v_readfirstlane_b32 s5, v1
	s_cmp_lg_u32 s5, 0
	s_cbranch_scc1 .Lfeat_done
	v_and_b32_e32 v1, 0x7f, v0
	v_lshl_or_b32 v1, s4, 7, v1
	s_mov_b32 s5, 0x20460
	v_cmp_gt_u32_e32 vcc, s5, v1
	s_mov_b64 s[6:7], vcc
	v_min_u32_e32 v1, 0x2045f, v1
	v_mul_u32_u24_e32 v5, 12, v1
	v_and_b32_e32 v6, 63, v0
	v_lshlrev_b32_e32 v6, 2, v6
	v_and_b32_e32 v7, 15, v0
	v_lshlrev_b32_e32 v7, 2, v7
	s_mov_b32 s5, 0xf0f0f0f1
	v_mul_hi_u32 v77, v1, s5
	v_lshrrev_b32_e32 v77, 4, v77
	v_lshl_add_u32 v77, v77, 4, v77
	v_sub_u32_e32 v77, v1, v77
	v_lshlrev_b32_e32 v77, 7, v77
	s_waitcnt lgkmcnt(0)
	global_load_dwordx3 v[2:4], v5, s[8:9]
	global_load_dword v72, v6, s[12:13]
	global_load_dword v73, v6, s[12:13] offset:256
	global_load_dword v74, v6, s[14:15]
	global_load_dword v75, v7, s[22:23]
	global_load_dword v76, v7, s[24:25]
	v_mov_b32_e32 v6, v77
	v_mul_u32_u24_e32 v1, 0x480, v1
	v_mov_b32_e32 v84, 0x378e98ab
	v_mov_b32_e32 v85, 0xb9c68948
	v_mov_b32_e32 v86, 0x3b7cd369
	v_mov_b32_e32 v87, 0xbcc618b2
	v_mov_b32_e32 v88, 0x3dda74e4
	v_mov_b32_e32 v89, 0x3f228afd
	v_mov_b32_e32 v90, 0x3ba10414
	v_mov_b32_e32 v91, 0x3e03c728
	v_mov_b32_e32 v92, 0xbfb8aa3b
	v_mov_b32_e32 v93, 0x42ce8ed0
	v_mov_b32_e32 v94, 0xc2b17218
	v_mov_b32_e32 v95, 0x7f800000
	s_brev_b32 s0, -2
	s_load_dwordx16 s[36:51], s[18:19], 0x0
	s_load_dwordx16 s[52:67], s[18:19], 0x40
	s_waitcnt lgkmcnt(0)
	v_mov_b32_e32 v8, s36
	v_mov_b32_e32 v9, s37
	v_mov_b32_e32 v10, s38
	v_mov_b32_e32 v11, s39
	v_mov_b32_e32 v12, s40
	v_mov_b32_e32 v13, s41
	v_mov_b32_e32 v14, s42
	v_mov_b32_e32 v15, s43
	v_mov_b32_e32 v16, s44
	v_mov_b32_e32 v17, s45
	v_mov_b32_e32 v18, s46
	v_mov_b32_e32 v19, s47
	v_mov_b32_e32 v20, s48
	v_mov_b32_e32 v21, s49
	v_mov_b32_e32 v22, s50
	v_mov_b32_e32 v23, s51
	v_mov_b32_e32 v24, s52
	v_mov_b32_e32 v25, s53
	v_mov_b32_e32 v26, s54
	v_mov_b32_e32 v27, s55
	v_mov_b32_e32 v28, s56
	v_mov_b32_e32 v29, s57
	v_mov_b32_e32 v30, s58
	v_mov_b32_e32 v31, s59
	v_mov_b32_e32 v32, s60
	v_mov_b32_e32 v33, s61
	v_mov_b32_e32 v34, s62
	v_mov_b32_e32 v35, s63
	v_mov_b32_e32 v36, s64
	v_mov_b32_e32 v37, s65
	v_mov_b32_e32 v38, s66
	v_mov_b32_e32 v39, s67
	s_waitcnt vmcnt(0)
	s_mov_b32 s10, 0
	v_mov_b32_e32 v7, 0x0
.Lfeat_loop_c:
	v_readlane_b32 s2, v72, s10
	v_readlane_b32 s3, v73, s10
	v_readlane_b32 s4, v74, s10
	ds_read_b128 v[40:43], v7 offset:0
	ds_read_b128 v[44:47], v7 offset:16
	ds_read_b128 v[48:51], v7 offset:32
	ds_read_b128 v[52:55], v7 offset:48
	ds_read_b128 v[56:59], v7 offset:64
	ds_read_b128 v[60:63], v7 offset:80
	ds_read_b128 v[64:67], v7 offset:96
	ds_read_b128 v[68:71], v7 offset:112
	v_add_u32_e32 v7, 0x80, v7
	v_mul_f32_e32 v77, s2, v2
	v_mul_f32_e32 v78, s3, v3
	v_add_f32_e32 v77, v77, v78
	v_add_f32_e32 v77, s4, v77
	v_mul_f32_e32 v78, 0x3f3504f3, v77
	v_mul_f32_e32 v79, v78, v78
	v_fmamk_f32 v81, v79, 0xba1345e1, v90
	v_fmaak_f32 v81, v79, v81, 0xbcdac9b8
	v_fmaak_f32 v81, v79, v81, 0x3de703be
	v_fmaak_f32 v81, v79, v81, 0xbec09330
	v_fmaak_f32 v81, v79, v81, 0x3e0375d0
	v_fma_f32 v81, |v78|, v81, |v78|
	v_cmp_nlt_f32_e64 vcc, |v78|, 1.0
	s_and_saveexec_b64 s[8:9], vcc
	s_cbranch_execz .Lfeat_nl_c0
	v_fma_f32 v82, |v78|, v84, v85
	v_fma_f32 v82, |v78|, v82, v86
	v_fma_f32 v82, |v78|, v82, v87
	v_fma_f32 v82, |v78|, v82, v88
	v_fma_f32 v82, |v78|, v82, v89
	v_fma_f32 v82, |v78|, v82, v91
	v_fma_f32 v82, |v78|, v82, |v78|
	v_mul_f32_e32 v83, 0xbfb8aa3b, v82
	v_fma_f32 v79, v82, v92, -v83
	v_rndne_f32_e32 v81, v83
	v_fmac_f32_e32 v79, 0xb2a5705f, v82
	v_sub_f32_e32 v83, v83, v81
	v_add_f32_e32 v83, v83, v79
	v_cvt_i32_f32_e32 v79, v81
	v_exp_f32_e32 v83, v83
	v_cmp_nlt_f32_e32 vcc, v93, v82
	v_ldexp_f32 v83, v83, v79
	s_nop 0
	v_cndmask_b32_e32 v83, 0, v83, vcc
	v_cmp_ngt_f32_e32 vcc, v94, v82
	s_nop 1
	v_cndmask_b32_e32 v82, v95, v83, vcc
	v_sub_f32_e32 v81, 1.0, v82
.Lfeat_nl_c0:
	s_mov_b64 exec, s[8:9]
	v_bfi_b32 v81, s0, v81, v78
	v_mul_f32_e32 v80, 0.5, v77
	v_add_f32_e32 v81, 1.0, v81
	v_mul_f32_e32 v80, v80, v81
	s_waitcnt lgkmcnt(0)
	v_fmac_f32_e32 v8, v40, v80
	v_fmac_f32_e32 v9, v41, v80
	v_fmac_f32_e32 v10, v42, v80
	v_fmac_f32_e32 v11, v43, v80
	v_fmac_f32_e32 v12, v44, v80
	v_fmac_f32_e32 v13, v45, v80
	v_fmac_f32_e32 v14, v46, v80
	v_fmac_f32_e32 v15, v47, v80
	v_fmac_f32_e32 v16, v48, v80
	v_fmac_f32_e32 v17, v49, v80
	v_fmac_f32_e32 v18, v50, v80
	v_fmac_f32_e32 v19, v51, v80
	v_fmac_f32_e32 v20, v52, v80
	v_fmac_f32_e32 v21, v53, v80
	v_fmac_f32_e32 v22, v54, v80
	v_fmac_f32_e32 v23, v55, v80
	v_fmac_f32_e32 v24, v56, v80
	v_fmac_f32_e32 v25, v57, v80
	v_fmac_f32_e32 v26, v58, v80
	v_fmac_f32_e32 v27, v59, v80
	v_fmac_f32_e32 v28, v60, v80
	v_fmac_f32_e32 v29, v61, v80
	v_fmac_f32_e32 v30, v62, v80
	v_fmac_f32_e32 v31, v63, v80
	v_fmac_f32_e32 v32, v64, v80
	v_fmac_f32_e32 v33, v65, v80
	v_fmac_f32_e32 v34, v66, v80
	v_fmac_f32_e32 v35, v67, v80
	v_fmac_f32_e32 v36, v68, v80
	v_fmac_f32_e32 v37, v69, v80
	v_fmac_f32_e32 v38, v70, v80
	v_fmac_f32_e32 v39, v71, v80
	s_add_u32 s5, s10, 1
	v_readlane_b32 s2, v72, s5
	v_readlane_b32 s3, v73, s5
	v_readlane_b32 s4, v74, s5
	ds_read_b128 v[40:43], v7 offset:0
	ds_read_b128 v[44:47], v7 offset:16
	ds_read_b128 v[48:51], v7 offset:32
	ds_read_b128 v[52:55], v7 offset:48
	ds_read_b128 v[56:59], v7 offset:64
	ds_read_b128 v[60:63], v7 offset:80
	ds_read_b128 v[64:67], v7 offset:96
	ds_read_b128 v[68:71], v7 offset:112
	v_add_u32_e32 v7, 0x80, v7
	v_mul_f32_e32 v77, s2, v2
	v_mul_f32_e32 v78, s3, v3
	v_add_f32_e32 v77, v77, v78
	v_add_f32_e32 v77, s4, v77
	v_mul_f32_e32 v78, 0x3f3504f3, v77
	v_mul_f32_e32 v79, v78, v78
	v_fmamk_f32 v81, v79, 0xba1345e1, v90
	v_fmaak_f32 v81, v79, v81, 0xbcdac9b8
	v_fmaak_f32 v81, v79, v81, 0x3de703be
	v_fmaak_f32 v81, v79, v81, 0xbec09330
	v_fmaak_f32 v81, v79, v81, 0x3e0375d0
	v_fma_f32 v81, |v78|, v81, |v78|
	v_cmp_nlt_f32_e64 vcc, |v78|, 1.0
	s_and_saveexec_b64 s[8:9], vcc
	s_cbranch_execz .Lfeat_nl_c1
	v_fma_f32 v82, |v78|, v84, v85
	v_fma_f32 v82, |v78|, v82, v86
	v_fma_f32 v82, |v78|, v82, v87
	v_fma_f32 v82, |v78|, v82, v88
	v_fma_f32 v82, |v78|, v82, v89
	v_fma_f32 v82, |v78|, v82, v91
	v_fma_f32 v82, |v78|, v82, |v78|
	v_mul_f32_e32 v83, 0xbfb8aa3b, v82
	v_fma_f32 v79, v82, v92, -v83
	v_rndne_f32_e32 v81, v83
	v_fmac_f32_e32 v79, 0xb2a5705f, v82
	v_sub_f32_e32 v83, v83, v81
	v_add_f32_e32 v83, v83, v79
	v_cvt_i32_f32_e32 v79, v81
	v_exp_f32_e32 v83, v83
	v_cmp_nlt_f32_e32 vcc, v93, v82
	v_ldexp_f32 v83, v83, v79
	s_nop 0
	v_cndmask_b32_e32 v83, 0, v83, vcc
	v_cmp_ngt_f32_e32 vcc, v94, v82
	s_nop 1
	v_cndmask_b32_e32 v82, v95, v83, vcc
	v_sub_f32_e32 v81, 1.0, v82
.Lfeat_nl_c1:
	s_mov_b64 exec, s[8:9]
	v_bfi_b32 v81, s0, v81, v78
	v_mul_f32_e32 v80, 0.5, v77
	v_add_f32_e32 v81, 1.0, v81
	v_mul_f32_e32 v80, v80, v81
	s_waitcnt lgkmcnt(0)
	v_fmac_f32_e32 v8, v40, v80
	v_fmac_f32_e32 v9, v41, v80
	v_fmac_f32_e32 v10, v42, v80
	v_fmac_f32_e32 v11, v43, v80
	v_fmac_f32_e32 v12, v44, v80
	v_fmac_f32_e32 v13, v45, v80
	v_fmac_f32_e32 v14, v46, v80
	v_fmac_f32_e32 v15, v47, v80
	v_fmac_f32_e32 v16, v48, v80
	v_fmac_f32_e32 v17, v49, v80
	v_fmac_f32_e32 v18, v50, v80
	v_fmac_f32_e32 v19, v51, v80
	v_fmac_f32_e32 v20, v52, v80
	v_fmac_f32_e32 v21, v53, v80
	v_fmac_f32_e32 v22, v54, v80
	v_fmac_f32_e32 v23, v55, v80
	v_fmac_f32_e32 v24, v56, v80
	v_fmac_f32_e32 v25, v57, v80
	v_fmac_f32_e32 v26, v58, v80
	v_fmac_f32_e32 v27, v59, v80
	v_fmac_f32_e32 v28, v60, v80
	v_fmac_f32_e32 v29, v61, v80
	v_fmac_f32_e32 v30, v62, v80
	v_fmac_f32_e32 v31, v63, v80
	v_fmac_f32_e32 v32, v64, v80
	v_fmac_f32_e32 v33, v65, v80
	v_fmac_f32_e32 v34, v66, v80
	v_fmac_f32_e32 v35, v67, v80
	v_fmac_f32_e32 v36, v68, v80
	v_fmac_f32_e32 v37, v69, v80
	v_fmac_f32_e32 v38, v70, v80
	v_fmac_f32_e32 v39, v71, v80
	s_add_u32 s10, s10, 2
	s_cmp_lt_u32 s10, 64
	s_cbranch_scc1 .Lfeat_loop_c
	global_load_dwordx4 v[40:43], v6, s[20:21] offset:0
	global_load_dwordx4 v[44:47], v6, s[20:21] offset:16
	global_load_dwordx4 v[48:51], v6, s[20:21] offset:32
	global_load_dwordx4 v[52:55], v6, s[20:21] offset:48
	global_load_dwordx4 v[56:59], v6, s[20:21] offset:64
	global_load_dwordx4 v[60:63], v6, s[20:21] offset:80
	global_load_dwordx4 v[64:67], v6, s[20:21] offset:96
	global_load_dwordx4 v[68:71], v6, s[20:21] offset:112
	s_waitcnt vmcnt(0)
	v_cmp_lt_f32_e32 vcc, 0.5, v4
	v_add_f32_e32 v8, v8, v40
	v_add_f32_e32 v9, v9, v41
	v_add_f32_e32 v10, v10, v42
	v_add_f32_e32 v11, v11, v43
	v_add_f32_e32 v12, v12, v44
	v_add_f32_e32 v13, v13, v45
	v_add_f32_e32 v14, v14, v46
	v_add_f32_e32 v15, v15, v47
	v_add_f32_e32 v16, v16, v48
	v_add_f32_e32 v17, v17, v49
	v_add_f32_e32 v18, v18, v50
	v_add_f32_e32 v19, v19, v51
	v_add_f32_e32 v20, v20, v52
	v_add_f32_e32 v21, v21, v53
	v_add_f32_e32 v22, v22, v54
	v_add_f32_e32 v23, v23, v55
	v_add_f32_e32 v24, v24, v56
	v_add_f32_e32 v25, v25, v57
	v_add_f32_e32 v26, v26, v58
	v_add_f32_e32 v27, v27, v59
	v_add_f32_e32 v28, v28, v60
	v_add_f32_e32 v29, v29, v61
	v_add_f32_e32 v30, v30, v62
	v_add_f32_e32 v31, v31, v63
	v_add_f32_e32 v32, v32, v64
	v_add_f32_e32 v33, v33, v65
	v_add_f32_e32 v34, v34, v66
	v_add_f32_e32 v35, v35, v67
	v_add_f32_e32 v36, v36, v68
	v_add_f32_e32 v37, v37, v69
	v_add_f32_e32 v38, v38, v70
	v_add_f32_e32 v39, v39, v71
	v_cndmask_b32_e32 v8, v40, v8, vcc
	v_cndmask_b32_e32 v9, v41, v9, vcc
	v_cndmask_b32_e32 v10, v42, v10, vcc
	v_cndmask_b32_e32 v11, v43, v11, vcc
	v_cndmask_b32_e32 v12, v44, v12, vcc
	v_cndmask_b32_e32 v13, v45, v13, vcc
	v_cndmask_b32_e32 v14, v46, v14, vcc
	v_cndmask_b32_e32 v15, v47, v15, vcc
	v_cndmask_b32_e32 v16, v48, v16, vcc
	v_cndmask_b32_e32 v17, v49, v17, vcc
	v_cndmask_b32_e32 v18, v50, v18, vcc
	v_cndmask_b32_e32 v19, v51, v19, vcc
	v_cndmask_b32_e32 v20, v52, v20, vcc
	v_cndmask_b32_e32 v21, v53, v21, vcc
	v_cndmask_b32_e32 v22, v54, v22, vcc
	v_cndmask_b32_e32 v23, v55, v23, vcc
	v_cndmask_b32_e32 v24, v56, v24, vcc
	v_cndmask_b32_e32 v25, v57, v25, vcc
	v_cndmask_b32_e32 v26, v58, v26, vcc
	v_cndmask_b32_e32 v27, v59, v27, vcc
	v_cndmask_b32_e32 v28, v60, v28, vcc
	v_cndmask_b32_e32 v29, v61, v29, vcc
	v_cndmask_b32_e32 v30, v62, v30, vcc
	v_cndmask_b32_e32 v31, v63, v31, vcc
	v_cndmask_b32_e32 v32, v64, v32, vcc
	v_cndmask_b32_e32 v33, v65, v33, vcc
	v_cndmask_b32_e32 v34, v66, v34, vcc
	v_cndmask_b32_e32 v35, v67, v35, vcc
	v_cndmask_b32_e32 v36, v68, v36, vcc
	v_cndmask_b32_e32 v37, v69, v37, vcc
	v_cndmask_b32_e32 v38, v70, v38, vcc
	v_cndmask_b32_e32 v39, v71, v39, vcc
	s_mov_b64 s[8:9], exec
	s_and_b64 exec, exec, s[6:7]
	v_cvt_pk_f16_f32 v80, v8, v9
	v_cvt_pk_f16_f32 v81, v10, v11
	v_cvt_pk_f16_f32 v82, v12, v13
	v_cvt_pk_f16_f32 v83, v14, v15
	global_store_dwordx4 v1, v[80:83], s[30:31] offset:1024
	s_nop 1
	v_cvt_pk_f16_f32 v80, v16, v17
	v_cvt_pk_f16_f32 v81, v18, v19
	v_cvt_pk_f16_f32 v82, v20, v21
	v_cvt_pk_f16_f32 v83, v22, v23
	global_store_dwordx4 v1, v[80:83], s[30:31] offset:1040
	s_nop 1
	v_cvt_pk_f16_f32 v80, v24, v25
	v_cvt_pk_f16_f32 v81, v26, v27
	v_cvt_pk_f16_f32 v82, v28, v29
	v_cvt_pk_f16_f32 v83, v30, v31
	global_store_dwordx4 v1, v[80:83], s[30:31] offset:1056
	s_nop 1
	v_cvt_pk_f16_f32 v80, v32, v33
	v_cvt_pk_f16_f32 v81, v34, v35
	v_cvt_pk_f16_f32 v82, v36, v37
	v_cvt_pk_f16_f32 v83, v38, v39
	global_store_dwordx4 v1, v[80:83], s[30:31] offset:1072
	s_mov_b64 exec, s[8:9]
	s_nop 1
	s_load_dwordx16 s[36:51], s[28:29], 0x0
	s_load_dwordx16 s[52:67], s[28:29], 0x40
	s_waitcnt lgkmcnt(0)
	v_mov_b32_e32 v8, s36
	v_mov_b32_e32 v9, s37
	v_mov_b32_e32 v10, s38
	v_mov_b32_e32 v11, s39
	v_mov_b32_e32 v12, s40
	v_mov_b32_e32 v13, s41
	v_mov_b32_e32 v14, s42
	v_mov_b32_e32 v15, s43
	v_mov_b32_e32 v16, s44
	v_mov_b32_e32 v17, s45
	v_mov_b32_e32 v18, s46
	v_mov_b32_e32 v19, s47
	v_mov_b32_e32 v20, s48
	v_mov_b32_e32 v21, s49
	v_mov_b32_e32 v22, s50
	v_mov_b32_e32 v23, s51
	v_mov_b32_e32 v24, s52
	v_mov_b32_e32 v25, s53
	v_mov_b32_e32 v26, s54
	v_mov_b32_e32 v27, s55
	v_mov_b32_e32 v28, s56
	v_mov_b32_e32 v29, s57
	v_mov_b32_e32 v30, s58
	v_mov_b32_e32 v31, s59
	v_mov_b32_e32 v32, s60
	v_mov_b32_e32 v33, s61
	v_mov_b32_e32 v34, s62
	v_mov_b32_e32 v35, s63
	v_mov_b32_e32 v36, s64
	v_mov_b32_e32 v37, s65
	v_mov_b32_e32 v38, s66
	v_mov_b32_e32 v39, s67
	s_mov_b32 s10, 0
	v_mov_b32_e32 v7, 0x2000
.Lfeat_loop_f:
	v_readlane_b32 s2, v75, s10
	v_readlane_b32 s3, v76, s10
	ds_read_b128 v[40:43], v7 offset:0
	ds_read_b128 v[44:47], v7 offset:16
	ds_read_b128 v[48:51], v7 offset:32
	ds_read_b128 v[52:55], v7 offset:48
	ds_read_b128 v[56:59], v7 offset:64
	ds_read_b128 v[60:63], v7 offset:80
	ds_read_b128 v[64:67], v7 offset:96
	ds_read_b128 v[68:71], v7 offset:112
	v_add_u32_e32 v7, 0x80, v7
	v_mov_b32_e32 v77, s3
	v_fmac_f32_e32 v77, s2, v4
	v_mul_f32_e32 v78, 0x3f3504f3, v77
	v_mul_f32_e32 v79, v78, v78
	v_fmamk_f32 v81, v79, 0xba1345e1, v90
	v_fmaak_f32 v81, v79, v81, 0xbcdac9b8
	v_fmaak_f32 v81, v79, v81, 0x3de703be
	v_fmaak_f32 v81, v79, v81, 0xbec09330
	v_fmaak_f32 v81, v79, v81, 0x3e0375d0
	v_fma_f32 v81, |v78|, v81, |v78|
	v_cmp_nlt_f32_e64 vcc, |v78|, 1.0
	s_and_saveexec_b64 s[8:9], vcc
	s_cbranch_execz .Lfeat_nl_f0
	v_fma_f32 v82, |v78|, v84, v85
	v_fma_f32 v82, |v78|, v82, v86
	v_fma_f32 v82, |v78|, v82, v87
	v_fma_f32 v82, |v78|, v82, v88
	v_fma_f32 v82, |v78|, v82, v89
	v_fma_f32 v82, |v78|, v82, v91
	v_fma_f32 v82, |v78|, v82, |v78|
	v_mul_f32_e32 v83, 0xbfb8aa3b, v82
	v_fma_f32 v79, v82, v92, -v83
	v_rndne_f32_e32 v81, v83
	v_fmac_f32_e32 v79, 0xb2a5705f, v82
	v_sub_f32_e32 v83, v83, v81
	v_add_f32_e32 v83, v83, v79
	v_cvt_i32_f32_e32 v79, v81
	v_exp_f32_e32 v83, v83
	v_cmp_nlt_f32_e32 vcc, v93, v82
	v_ldexp_f32 v83, v83, v79
	s_nop 0
	v_cndmask_b32_e32 v83, 0, v83, vcc
	v_cmp_ngt_f32_e32 vcc, v94, v82
	s_nop 1
	v_cndmask_b32_e32 v82, v95, v83, vcc
	v_sub_f32_e32 v81, 1.0, v82
.Lfeat_nl_f0:
	s_mov_b64 exec, s[8:9]
	v_bfi_b32 v81, s0, v81, v78
	v_mul_f32_e32 v80, 0.5, v77
	v_add_f32_e32 v81, 1.0, v81
	v_mul_f32_e32 v80, v80, v81
	s_waitcnt lgkmcnt(0)
	v_fmac_f32_e32 v8, v40, v80
	v_fmac_f32_e32 v9, v41, v80
	v_fmac_f32_e32 v10, v42, v80
	v_fmac_f32_e32 v11, v43, v80
	v_fmac_f32_e32 v12, v44, v80
	v_fmac_f32_e32 v13, v45, v80
	v_fmac_f32_e32 v14, v46, v80
	v_fmac_f32_e32 v15, v47, v80
	v_fmac_f32_e32 v16, v48, v80
	v_fmac_f32_e32 v17, v49, v80
	v_fmac_f32_e32 v18, v50, v80
	v_fmac_f32_e32 v19, v51, v80
	v_fmac_f32_e32 v20, v52, v80
	v_fmac_f32_e32 v21, v53, v80
	v_fmac_f32_e32 v22, v54, v80
	v_fmac_f32_e32 v23, v55, v80
	v_fmac_f32_e32 v24, v56, v80
	v_fmac_f32_e32 v25, v57, v80
	v_fmac_f32_e32 v26, v58, v80
	v_fmac_f32_e32 v27, v59, v80
	v_fmac_f32_e32 v28, v60, v80
	v_fmac_f32_e32 v29, v61, v80
	v_fmac_f32_e32 v30, v62, v80
	v_fmac_f32_e32 v31, v63, v80
	v_fmac_f32_e32 v32, v64, v80
	v_fmac_f32_e32 v33, v65, v80
	v_fmac_f32_e32 v34, v66, v80
	v_fmac_f32_e32 v35, v67, v80
	v_fmac_f32_e32 v36, v68, v80
	v_fmac_f32_e32 v37, v69, v80
	v_fmac_f32_e32 v38, v70, v80
	v_fmac_f32_e32 v39, v71, v80
	s_add_u32 s5, s10, 1
	v_readlane_b32 s2, v75, s5
	v_readlane_b32 s3, v76, s5
	ds_read_b128 v[40:43], v7 offset:0
	ds_read_b128 v[44:47], v7 offset:16
	ds_read_b128 v[48:51], v7 offset:32
	ds_read_b128 v[52:55], v7 offset:48
	ds_read_b128 v[56:59], v7 offset:64
	ds_read_b128 v[60:63], v7 offset:80
	ds_read_b128 v[64:67], v7 offset:96
	ds_read_b128 v[68:71], v7 offset:112
	v_add_u32_e32 v7, 0x80, v7
	v_mov_b32_e32 v77, s3
	v_fmac_f32_e32 v77, s2, v4
	v_mul_f32_e32 v78, 0x3f3504f3, v77
	v_mul_f32_e32 v79, v78, v78
	v_fmamk_f32 v81, v79, 0xba1345e1, v90
	v_fmaak_f32 v81, v79, v81, 0xbcdac9b8
	v_fmaak_f32 v81, v79, v81, 0x3de703be
	v_fmaak_f32 v81, v79, v81, 0xbec09330
	v_fmaak_f32 v81, v79, v81, 0x3e0375d0
	v_fma_f32 v81, |v78|, v81, |v78|
	v_cmp_nlt_f32_e64 vcc, |v78|, 1.0
	s_and_saveexec_b64 s[8:9], vcc
	s_cbranch_execz .Lfeat_nl_f1
	v_fma_f32 v82, |v78|, v84, v85
	v_fma_f32 v82, |v78|, v82, v86
	v_fma_f32 v82, |v78|, v82, v87
	v_fma_f32 v82, |v78|, v82, v88
	v_fma_f32 v82, |v78|, v82, v89
	v_fma_f32 v82, |v78|, v82, v91
	v_fma_f32 v82, |v78|, v82, |v78|
	v_mul_f32_e32 v83, 0xbfb8aa3b, v82
	v_fma_f32 v79, v82, v92, -v83
	v_rndne_f32_e32 v81, v83
	v_fmac_f32_e32 v79, 0xb2a5705f, v82
	v_sub_f32_e32 v83, v83, v81
	v_add_f32_e32 v83, v83, v79
	v_cvt_i32_f32_e32 v79, v81
	v_exp_f32_e32 v83, v83
	v_cmp_nlt_f32_e32 vcc, v93, v82
	v_ldexp_f32 v83, v83, v79
	s_nop 0
	v_cndmask_b32_e32 v83, 0, v83, vcc
	v_cmp_ngt_f32_e32 vcc, v94, v82
	s_nop 1
	v_cndmask_b32_e32 v82, v95, v83, vcc
	v_sub_f32_e32 v81, 1.0, v82
.Lfeat_nl_f1:
	s_mov_b64 exec, s[8:9]
	v_bfi_b32 v81, s0, v81, v78
	v_mul_f32_e32 v80, 0.5, v77
	v_add_f32_e32 v81, 1.0, v81
	v_mul_f32_e32 v80, v80, v81
	s_waitcnt lgkmcnt(0)
	v_fmac_f32_e32 v8, v40, v80
	v_fmac_f32_e32 v9, v41, v80
	v_fmac_f32_e32 v10, v42, v80
	v_fmac_f32_e32 v11, v43, v80
	v_fmac_f32_e32 v12, v44, v80
	v_fmac_f32_e32 v13, v45, v80
	v_fmac_f32_e32 v14, v46, v80
	v_fmac_f32_e32 v15, v47, v80
	v_fmac_f32_e32 v16, v48, v80
	v_fmac_f32_e32 v17, v49, v80
	v_fmac_f32_e32 v18, v50, v80
	v_fmac_f32_e32 v19, v51, v80
	v_fmac_f32_e32 v20, v52, v80
	v_fmac_f32_e32 v21, v53, v80
	v_fmac_f32_e32 v22, v54, v80
	v_fmac_f32_e32 v23, v55, v80
	v_fmac_f32_e32 v24, v56, v80
	v_fmac_f32_e32 v25, v57, v80
	v_fmac_f32_e32 v26, v58, v80
	v_fmac_f32_e32 v27, v59, v80
	v_fmac_f32_e32 v28, v60, v80
	v_fmac_f32_e32 v29, v61, v80
	v_fmac_f32_e32 v30, v62, v80
	v_fmac_f32_e32 v31, v63, v80
	v_fmac_f32_e32 v32, v64, v80
	v_fmac_f32_e32 v33, v65, v80
	v_fmac_f32_e32 v34, v66, v80
	v_fmac_f32_e32 v35, v67, v80
	v_fmac_f32_e32 v36, v68, v80
	v_fmac_f32_e32 v37, v69, v80
	v_fmac_f32_e32 v38, v70, v80
	v_fmac_f32_e32 v39, v71, v80
	s_add_u32 s10, s10, 2
	s_cmp_lt_u32 s10, 16
	s_cbranch_scc1 .Lfeat_loop_f
	s_and_b64 exec, exec, s[6:7]
	v_cvt_pk_f16_f32 v80, v8, v9
	v_cvt_pk_f16_f32 v81, v10, v11
	v_cvt_pk_f16_f32 v82, v12, v13
	v_cvt_pk_f16_f32 v83, v14, v15
	global_store_dwordx4 v1, v[80:83], s[30:31] offset:1088
	s_nop 1
	v_cvt_pk_f16_f32 v80, v16, v17
	v_cvt_pk_f16_f32 v81, v18, v19
	v_cvt_pk_f16_f32 v82, v20, v21
	v_cvt_pk_f16_f32 v83, v22, v23
	global_store_dwordx4 v1, v[80:83], s[30:31] offset:1104
	s_nop 1
	v_cvt_pk_f16_f32 v80, v24, v25
	v_cvt_pk_f16_f32 v81, v26, v27
	v_cvt_pk_f16_f32 v82, v28, v29
	v_cvt_pk_f16_f32 v83, v30, v31
	global_store_dwordx4 v1, v[80:83], s[30:31] offset:1120
	s_nop 1
	v_cvt_pk_f16_f32 v80, v32, v33
	v_cvt_pk_f16_f32 v81, v34, v35
	v_cvt_pk_f16_f32 v82, v36, v37
	v_cvt_pk_f16_f32 v83, v38, v39
	global_store_dwordx4 v1, v[80:83], s[30:31] offset:1136
.Lfeat_done:
	s_endpgm
.LBB0_79:
	v_readlane_b32 s4, v83, 17
	v_readlane_b32 s5, v83, 18
	s_or_b64 exec, exec, s[4:5]
	s_mov_b64 s[4:5], 0

.LBB0_133:
	s_or_b64 exec, exec, s[0:1]
	s_mul_i32 s3, s3, 12
	s_sub_i32 s0, s2, s3
	v_and_b32_e32 v24, 0x7f, v0
	v_lshl_or_b32 v2, s0, 7, v24
	s_mov_b32 s0, 0x2aaaaaab
	v_mul_hi_i32 v1, v2, s0
	v_lshrrev_b32_e32 v4, 31, v1
	v_ashrrev_i32_e32 v1, 5, v1
	v_add_u32_e32 v1, v1, v4
	s_movk_i32 s0, 0xc0
	v_mul_lo_u32 v4, v1, s0
	v_sub_u32_e32 v4, v2, v4
	v_lshrrev_b32_e32 v3, 7, v0
	v_and_b32_e32 v22, 63, v0
	v_and_b32_e32 v0, 0xffffffc0, v4
	v_mov_b32_e32 v5, s50
	v_mov_b32_e32 v6, s48
	v_cmp_eq_u32_e32 vcc, 64, v0
	v_cmp_gt_u32_e64 s[0:1], 64, v4
	v_mov_b32_e32 v4, s46
	v_cndmask_b32_e32 v0, v5, v6, vcc
	v_lshlrev_b32_e32 v23, 6, v1
	v_mov_b32_e32 v5, s51
	v_mov_b32_e32 v6, s49
	v_cndmask_b32_e64 v16, v0, v4, s[0:1]
	v_lshl_add_u32 v0, v3, 17, v23
	v_cndmask_b32_e32 v5, v5, v6, vcc
	v_mov_b32_e32 v6, s47
	v_or_b32_e32 v18, v0, v22
	v_cndmask_b32_e64 v17, v5, v6, s[0:1]
	v_add_u32_e32 v0, 0xe00, v18
	v_add_u32_e32 v4, 0xc00, v18
	v_add_u32_e32 v6, 0xa00, v18
	v_add_u32_e32 v8, 0x800, v18
	v_add_u32_e32 v10, 0x600, v18
	v_add_u32_e32 v12, 0x400, v18
	v_add_u32_e32 v14, 0x200, v18
	v_ashrrev_i32_e32 v1, 31, v0
	v_ashrrev_i32_e32 v5, 31, v4
	v_ashrrev_i32_e32 v7, 31, v6
	v_ashrrev_i32_e32 v9, 31, v8
	v_ashrrev_i32_e32 v11, 31, v10
	v_ashrrev_i32_e32 v13, 31, v12
	v_ashrrev_i32_e32 v15, 31, v14
	v_ashrrev_i32_e32 v19, 31, v18
	v_lshl_add_u64 v[0:1], v[0:1], 2, v[16:17]
	v_lshl_add_u64 v[4:5], v[4:5], 2, v[16:17]
	v_lshl_add_u64 v[6:7], v[6:7], 2, v[16:17]
	v_lshl_add_u64 v[8:9], v[8:9], 2, v[16:17]
	v_lshl_add_u64 v[10:11], v[10:11], 2, v[16:17]
	v_lshl_add_u64 v[12:13], v[12:13], 2, v[16:17]
	v_lshl_add_u64 v[14:15], v[14:15], 2, v[16:17]
	v_lshl_add_u64 v[16:17], v[18:19], 2, v[16:17]
	v_mov_b32_e32 v18, 0
	v_lshlrev_b32_e32 v25, 10, v3
	s_mov_b64 s[2:3], 0
	v_mov_b32_e32 v19, v18
	v_mov_b32_e32 v20, v18
	v_mov_b32_e32 v21, v18
	s_waitcnt lgkmcnt(0)
	s_barrier
	s_mov_b32 s2, 0x4000
	s_mov_b32 s3, 0
	s_mov_b32 s8, 7
	global_load_dword v26, v[16:17], off
	global_load_dword v27, v[14:15], off
	global_load_dword v28, v[12:13], off
	global_load_dword v29, v[10:11], off
	global_load_dword v30, v[8:9], off
	global_load_dword v31, v[6:7], off
	global_load_dword v32, v[4:5], off
	global_load_dword v33, v[0:1], off
	v_lshl_add_u64 v[16:17], v[16:17], 0, s[2:3]
	v_lshl_add_u64 v[14:15], v[14:15], 0, s[2:3]
	v_lshl_add_u64 v[12:13], v[12:13], 0, s[2:3]
	v_lshl_add_u64 v[10:11], v[10:11], 0, s[2:3]
	v_lshl_add_u64 v[8:9], v[8:9], 0, s[2:3]
	v_lshl_add_u64 v[6:7], v[6:7], 0, s[2:3]
	v_lshl_add_u64 v[4:5], v[4:5], 0, s[2:3]
	v_lshl_add_u64 v[0:1], v[0:1], 0, s[2:3]
	global_load_dword v34, v[16:17], off
	global_load_dword v35, v[14:15], off
	global_load_dword v36, v[12:13], off
	global_load_dword v37, v[10:11], off
	global_load_dword v38, v[8:9], off
	global_load_dword v39, v[6:7], off
	global_load_dword v40, v[4:5], off
	global_load_dword v41, v[0:1], off
	v_lshl_add_u64 v[16:17], v[16:17], 0, s[2:3]
	v_lshl_add_u64 v[14:15], v[14:15], 0, s[2:3]
	v_lshl_add_u64 v[12:13], v[12:13], 0, s[2:3]
	v_lshl_add_u64 v[10:11], v[10:11], 0, s[2:3]
	v_lshl_add_u64 v[8:9], v[8:9], 0, s[2:3]
	v_lshl_add_u64 v[6:7], v[6:7], 0, s[2:3]
	v_lshl_add_u64 v[4:5], v[4:5], 0, s[2:3]
	v_lshl_add_u64 v[0:1], v[0:1], 0, s[2:3]
	global_load_dword v42, v[16:17], off
	global_load_dword v43, v[14:15], off
	global_load_dword v44, v[12:13], off
	global_load_dword v45, v[10:11], off
	global_load_dword v46, v[8:9], off
	global_load_dword v47, v[6:7], off
	global_load_dword v48, v[4:5], off
	global_load_dword v49, v[0:1], off
	v_lshl_add_u64 v[16:17], v[16:17], 0, s[2:3]
	v_lshl_add_u64 v[14:15], v[14:15], 0, s[2:3]
	v_lshl_add_u64 v[12:13], v[12:13], 0, s[2:3]
	v_lshl_add_u64 v[10:11], v[10:11], 0, s[2:3]
	v_lshl_add_u64 v[8:9], v[8:9], 0, s[2:3]
	v_lshl_add_u64 v[6:7], v[6:7], 0, s[2:3]
	v_lshl_add_u64 v[4:5], v[4:5], 0, s[2:3]
	v_lshl_add_u64 v[0:1], v[0:1], 0, s[2:3]
	global_load_dword v50, v[16:17], off
	global_load_dword v51, v[14:15], off
	global_load_dword v52, v[12:13], off
	global_load_dword v53, v[10:11], off
	global_load_dword v54, v[8:9], off
	global_load_dword v55, v[6:7], off
	global_load_dword v56, v[4:5], off
	global_load_dword v57, v[0:1], off
	v_lshl_add_u64 v[16:17], v[16:17], 0, s[2:3]
	v_lshl_add_u64 v[14:15], v[14:15], 0, s[2:3]
	v_lshl_add_u64 v[12:13], v[12:13], 0, s[2:3]
	v_lshl_add_u64 v[10:11], v[10:11], 0, s[2:3]
	v_lshl_add_u64 v[8:9], v[8:9], 0, s[2:3]
	v_lshl_add_u64 v[6:7], v[6:7], 0, s[2:3]
	v_lshl_add_u64 v[4:5], v[4:5], 0, s[2:3]
	v_lshl_add_u64 v[0:1], v[0:1], 0, s[2:3]
.Lfold_loop:
	ds_read_b128 v[58:61], v25
	ds_read_b128 v[62:65], v25 offset:16
	ds_read_b128 v[66:69], v25 offset:2048
	ds_read_b128 v[70:73], v25 offset:2064
	ds_read_b128 v[74:77], v25 offset:4096
	ds_read_b128 v[78:81], v25 offset:4112
	ds_read_b128 v[84:87], v25 offset:6144
	ds_read_b128 v[88:91], v25 offset:6160
	v_add_u32_e32 v25, 32, v25
	s_waitcnt vmcnt(24)
	s_waitcnt lgkmcnt(0)
	v_fmac_f32_e32 v18, v26, v58
	v_fmac_f32_e32 v19, v26, v66
	v_fmac_f32_e32 v20, v26, v74
	v_fmac_f32_e32 v21, v26, v84
	v_fmac_f32_e32 v18, v27, v59
	v_fmac_f32_e32 v19, v27, v67
	v_fmac_f32_e32 v20, v27, v75
	v_fmac_f32_e32 v21, v27, v85
	v_fmac_f32_e32 v18, v28, v60
	v_fmac_f32_e32 v19, v28, v68
	v_fmac_f32_e32 v20, v28, v76
	v_fmac_f32_e32 v21, v28, v86
	v_fmac_f32_e32 v18, v29, v61
	v_fmac_f32_e32 v19, v29, v69
	v_fmac_f32_e32 v20, v29, v77
	v_fmac_f32_e32 v21, v29, v87
	v_fmac_f32_e32 v18, v30, v62
	v_fmac_f32_e32 v19, v30, v70
	v_fmac_f32_e32 v20, v30, v78
	v_fmac_f32_e32 v21, v30, v88
	v_fmac_f32_e32 v18, v31, v63
	v_fmac_f32_e32 v19, v31, v71
	v_fmac_f32_e32 v20, v31, v79
	v_fmac_f32_e32 v21, v31, v89
	v_fmac_f32_e32 v18, v32, v64
	v_fmac_f32_e32 v19, v32, v72
	v_fmac_f32_e32 v20, v32, v80
	v_fmac_f32_e32 v21, v32, v90
	v_fmac_f32_e32 v18, v33, v65
	v_fmac_f32_e32 v19, v33, v73
	v_fmac_f32_e32 v20, v33, v81
	v_fmac_f32_e32 v21, v33, v91
	global_load_dword v26, v[16:17], off
	global_load_dword v27, v[14:15], off
	global_load_dword v28, v[12:13], off
	global_load_dword v29, v[10:11], off
	global_load_dword v30, v[8:9], off
	global_load_dword v31, v[6:7], off
	global_load_dword v32, v[4:5], off
	global_load_dword v33, v[0:1], off
	v_lshl_add_u64 v[16:17], v[16:17], 0, s[2:3]
	v_lshl_add_u64 v[14:15], v[14:15], 0, s[2:3]
	v_lshl_add_u64 v[12:13], v[12:13], 0, s[2:3]
	v_lshl_add_u64 v[10:11], v[10:11], 0, s[2:3]
	v_lshl_add_u64 v[8:9], v[8:9], 0, s[2:3]
	v_lshl_add_u64 v[6:7], v[6:7], 0, s[2:3]
	v_lshl_add_u64 v[4:5], v[4:5], 0, s[2:3]
	v_lshl_add_u64 v[0:1], v[0:1], 0, s[2:3]
	ds_read_b128 v[58:61], v25
	ds_read_b128 v[62:65], v25 offset:16
	ds_read_b128 v[66:69], v25 offset:2048
	ds_read_b128 v[70:73], v25 offset:2064
	ds_read_b128 v[74:77], v25 offset:4096
	ds_read_b128 v[78:81], v25 offset:4112
	ds_read_b128 v[84:87], v25 offset:6144
	ds_read_b128 v[88:91], v25 offset:6160
	v_add_u32_e32 v25, 32, v25
	s_waitcnt vmcnt(24)
	s_waitcnt lgkmcnt(0)
	v_fmac_f32_e32 v18, v34, v58
	v_fmac_f32_e32 v19, v34, v66
	v_fmac_f32_e32 v20, v34, v74
	v_fmac_f32_e32 v21, v34, v84
	v_fmac_f32_e32 v18, v35, v59
	v_fmac_f32_e32 v19, v35, v67
	v_fmac_f32_e32 v20, v35, v75
	v_fmac_f32_e32 v21, v35, v85
	v_fmac_f32_e32 v18, v36, v60
	v_fmac_f32_e32 v19, v36, v68
	v_fmac_f32_e32 v20, v36, v76
	v_fmac_f32_e32 v21, v36, v86
	v_fmac_f32_e32 v18, v37, v61
	v_fmac_f32_e32 v19, v37, v69
	v_fmac_f32_e32 v20, v37, v77
	v_fmac_f32_e32 v21, v37, v87
	v_fmac_f32_e32 v18, v38, v62
	v_fmac_f32_e32 v19, v38, v70
	v_fmac_f32_e32 v20, v38, v78
	v_fmac_f32_e32 v21, v38, v88
	v_fmac_f32_e32 v18, v39, v63
	v_fmac_f32_e32 v19, v39, v71
	v_fmac_f32_e32 v20, v39, v79
	v_fmac_f32_e32 v21, v39, v89
	v_fmac_f32_e32 v18, v40, v64
	v_fmac_f32_e32 v19, v40, v72
	v_fmac_f32_e32 v20, v40, v80
	v_fmac_f32_e32 v21, v40, v90
	v_fmac_f32_e32 v18, v41, v65
	v_fmac_f32_e32 v19, v41, v73
	v_fmac_f32_e32 v20, v41, v81
	v_fmac_f32_e32 v21, v41, v91
	global_load_dword v34, v[16:17], off
	global_load_dword v35, v[14:15], off
	global_load_dword v36, v[12:13], off
	global_load_dword v37, v[10:11], off
	global_load_dword v38, v[8:9], off
	global_load_dword v39, v[6:7], off
	global_load_dword v40, v[4:5], off
	global_load_dword v41, v[0:1], off
	v_lshl_add_u64 v[16:17], v[16:17], 0, s[2:3]
	v_lshl_add_u64 v[14:15], v[14:15], 0, s[2:3]
	v_lshl_add_u64 v[12:13], v[12:13], 0, s[2:3]
	v_lshl_add_u64 v[10:11], v[10:11], 0, s[2:3]
	v_lshl_add_u64 v[8:9], v[8:9], 0, s[2:3]
	v_lshl_add_u64 v[6:7], v[6:7], 0, s[2:3]
	v_lshl_add_u64 v[4:5], v[4:5], 0, s[2:3]
	v_lshl_add_u64 v[0:1], v[0:1], 0, s[2:3]
	ds_read_b128 v[58:61], v25
	ds_read_b128 v[62:65], v25 offset:16
	ds_read_b128 v[66:69], v25 offset:2048
	ds_read_b128 v[70:73], v25 offset:2064
	ds_read_b128 v[74:77], v25 offset:4096
	ds_read_b128 v[78:81], v25 offset:4112
	ds_read_b128 v[84:87], v25 offset:6144
	ds_read_b128 v[88:91], v25 offset:6160
	v_add_u32_e32 v25, 32, v25
	s_waitcnt vmcnt(24)
	s_waitcnt lgkmcnt(0)
	v_fmac_f32_e32 v18, v42, v58
	v_fmac_f32_e32 v19, v42, v66
	v_fmac_f32_e32 v20, v42, v74
	v_fmac_f32_e32 v21, v42, v84
	v_fmac_f32_e32 v18, v43, v59
	v_fmac_f32_e32 v19, v43, v67
	v_fmac_f32_e32 v20, v43, v75
	v_fmac_f32_e32 v21, v43, v85
	v_fmac_f32_e32 v18, v44, v60
	v_fmac_f32_e32 v19, v44, v68
	v_fmac_f32_e32 v20, v44, v76
	v_fmac_f32_e32 v21, v44, v86
	v_fmac_f32_e32 v18, v45, v61
	v_fmac_f32_e32 v19, v45, v69
	v_fmac_f32_e32 v20, v45, v77
	v_fmac_f32_e32 v21, v45, v87
	v_fmac_f32_e32 v18, v46, v62
	v_fmac_f32_e32 v19, v46, v70
	v_fmac_f32_e32 v20, v46, v78
	v_fmac_f32_e32 v21, v46, v88
	v_fmac_f32_e32 v18, v47, v63
	v_fmac_f32_e32 v19, v47, v71
	v_fmac_f32_e32 v20, v47, v79
	v_fmac_f32_e32 v21, v47, v89
	v_fmac_f32_e32 v18, v48, v64
	v_fmac_f32_e32 v19, v48, v72
	v_fmac_f32_e32 v20, v48, v80
	v_fmac_f32_e32 v21, v48, v90
	v_fmac_f32_e32 v18, v49, v65
	v_fmac_f32_e32 v19, v49, v73
	v_fmac_f32_e32 v20, v49, v81
	v_fmac_f32_e32 v21, v49, v91
	global_load_dword v42, v[16:17], off
	global_load_dword v43, v[14:15], off
	global_load_dword v44, v[12:13], off
	global_load_dword v45, v[10:11], off
	global_load_dword v46, v[8:9], off
	global_load_dword v47, v[6:7], off
	global_load_dword v48, v[4:5], off
	global_load_dword v49, v[0:1], off
	v_lshl_add_u64 v[16:17], v[16:17], 0, s[2:3]
	v_lshl_add_u64 v[14:15], v[14:15], 0, s[2:3]
	v_lshl_add_u64 v[12:13], v[12:13], 0, s[2:3]
	v_lshl_add_u64 v[10:11], v[10:11], 0, s[2:3]
	v_lshl_add_u64 v[8:9], v[8:9], 0, s[2:3]
	v_lshl_add_u64 v[6:7], v[6:7], 0, s[2:3]
	v_lshl_add_u64 v[4:5], v[4:5], 0, s[2:3]
	v_lshl_add_u64 v[0:1], v[0:1], 0, s[2:3]
	ds_read_b128 v[58:61], v25
	ds_read_b128 v[62:65], v25 offset:16
	ds_read_b128 v[66:69], v25 offset:2048
	ds_read_b128 v[70:73], v25 offset:2064
	ds_read_b128 v[74:77], v25 offset:4096
	ds_read_b128 v[78:81], v25 offset:4112
	ds_read_b128 v[84:87], v25 offset:6144
	ds_read_b128 v[88:91], v25 offset:6160
	v_add_u32_e32 v25, 32, v25
	s_waitcnt vmcnt(24)
	s_waitcnt lgkmcnt(0)
	v_fmac_f32_e32 v18, v50, v58
	v_fmac_f32_e32 v19, v50, v66
	v_fmac_f32_e32 v20, v50, v74
	v_fmac_f32_e32 v21, v50, v84
	v_fmac_f32_e32 v18, v51, v59
	v_fmac_f32_e32 v19, v51, v67
	v_fmac_f32_e32 v20, v51, v75
	v_fmac_f32_e32 v21, v51, v85
	v_fmac_f32_e32 v18, v52, v60
	v_fmac_f32_e32 v19, v52, v68
	v_fmac_f32_e32 v20, v52, v76
	v_fmac_f32_e32 v21, v52, v86
	v_fmac_f32_e32 v18, v53, v61
	v_fmac_f32_e32 v19, v53, v69
	v_fmac_f32_e32 v20, v53, v77
	v_fmac_f32_e32 v21, v53, v87
	v_fmac_f32_e32 v18, v54, v62
	v_fmac_f32_e32 v19, v54, v70
	v_fmac_f32_e32 v20, v54, v78
	v_fmac_f32_e32 v21, v54, v88
	v_fmac_f32_e32 v18, v55, v63
	v_fmac_f32_e32 v19, v55, v71
	v_fmac_f32_e32 v20, v55, v79
	v_fmac_f32_e32 v21, v55, v89
	v_fmac_f32_e32 v18, v56, v64
	v_fmac_f32_e32 v19, v56, v72
	v_fmac_f32_e32 v20, v56, v80
	v_fmac_f32_e32 v21, v56, v90
	v_fmac_f32_e32 v18, v57, v65
	v_fmac_f32_e32 v19, v57, v73
	v_fmac_f32_e32 v20, v57, v81
	v_fmac_f32_e32 v21, v57, v91
	global_load_dword v50, v[16:17], off
	global_load_dword v51, v[14:15], off
	global_load_dword v52, v[12:13], off
	global_load_dword v53, v[10:11], off
	global_load_dword v54, v[8:9], off
	global_load_dword v55, v[6:7], off
	global_load_dword v56, v[4:5], off
	global_load_dword v57, v[0:1], off
	v_lshl_add_u64 v[16:17], v[16:17], 0, s[2:3]
	v_lshl_add_u64 v[14:15], v[14:15], 0, s[2:3]
	v_lshl_add_u64 v[12:13], v[12:13], 0, s[2:3]
	v_lshl_add_u64 v[10:11], v[10:11], 0, s[2:3]
	v_lshl_add_u64 v[8:9], v[8:9], 0, s[2:3]
	v_lshl_add_u64 v[6:7], v[6:7], 0, s[2:3]
	v_lshl_add_u64 v[4:5], v[4:5], 0, s[2:3]
	v_lshl_add_u64 v[0:1], v[0:1], 0, s[2:3]
	s_sub_u32 s8, s8, 1
	s_cmp_lg_u32 s8, 0
	s_cbranch_scc1 .Lfold_loop
	ds_read_b128 v[58:61], v25
	ds_read_b128 v[62:65], v25 offset:16
	ds_read_b128 v[66:69], v25 offset:2048
	ds_read_b128 v[70:73], v25 offset:2064
	ds_read_b128 v[74:77], v25 offset:4096
	ds_read_b128 v[78:81], v25 offset:4112
	ds_read_b128 v[84:87], v25 offset:6144
	ds_read_b128 v[88:91], v25 offset:6160
	v_add_u32_e32 v25, 32, v25
	s_waitcnt vmcnt(24)
	s_waitcnt lgkmcnt(0)
	v_fmac_f32_e32 v18, v26, v58
	v_fmac_f32_e32 v19, v26, v66
	v_fmac_f32_e32 v20, v26, v74
	v_fmac_f32_e32 v21, v26, v84
	v_fmac_f32_e32 v18, v27, v59
	v_fmac_f32_e32 v19, v27, v67
	v_fmac_f32_e32 v20, v27, v75
	v_fmac_f32_e32 v21, v27, v85
	v_fmac_f32_e32 v18, v28, v60
	v_fmac_f32_e32 v19, v28, v68
	v_fmac_f32_e32 v20, v28, v76
	v_fmac_f32_e32 v21, v28, v86
	v_fmac_f32_e32 v18, v29, v61
	v_fmac_f32_e32 v19, v29, v69
	v_fmac_f32_e32 v20, v29, v77
	v_fmac_f32_e32 v21, v29, v87
	v_fmac_f32_e32 v18, v30, v62
	v_fmac_f32_e32 v19, v30, v70
	v_fmac_f32_e32 v20, v30, v78
	v_fmac_f32_e32 v21, v30, v88
	v_fmac_f32_e32 v18, v31, v63
	v_fmac_f32_e32 v19, v31, v71
	v_fmac_f32_e32 v20, v31, v79
	v_fmac_f32_e32 v21, v31, v89
	v_fmac_f32_e32 v18, v32, v64
	v_fmac_f32_e32 v19, v32, v72
	v_fmac_f32_e32 v20, v32, v80
	v_fmac_f32_e32 v21, v32, v90
	v_fmac_f32_e32 v18, v33, v65
	v_fmac_f32_e32 v19, v33, v73
	v_fmac_f32_e32 v20, v33, v81
	v_fmac_f32_e32 v21, v33, v91
	ds_read_b128 v[58:61], v25
	ds_read_b128 v[62:65], v25 offset:16
	ds_read_b128 v[66:69], v25 offset:2048
	ds_read_b128 v[70:73], v25 offset:2064
	ds_read_b128 v[74:77], v25 offset:4096
	ds_read_b128 v[78:81], v25 offset:4112
	ds_read_b128 v[84:87], v25 offset:6144
	ds_read_b128 v[88:91], v25 offset:6160
	v_add_u32_e32 v25, 32, v25
	s_waitcnt vmcnt(16)
	s_waitcnt lgkmcnt(0)
	v_fmac_f32_e32 v18, v34, v58
	v_fmac_f32_e32 v19, v34, v66
	v_fmac_f32_e32 v20, v34, v74
	v_fmac_f32_e32 v21, v34, v84
	v_fmac_f32_e32 v18, v35, v59
	v_fmac_f32_e32 v19, v35, v67
	v_fmac_f32_e32 v20, v35, v75
	v_fmac_f32_e32 v21, v35, v85
	v_fmac_f32_e32 v18, v36, v60
	v_fmac_f32_e32 v19, v36, v68
	v_fmac_f32_e32 v20, v36, v76
	v_fmac_f32_e32 v21, v36, v86
	v_fmac_f32_e32 v18, v37, v61
	v_fmac_f32_e32 v19, v37, v69
	v_fmac_f32_e32 v20, v37, v77
	v_fmac_f32_e32 v21, v37, v87
	v_fmac_f32_e32 v18, v38, v62
	v_fmac_f32_e32 v19, v38, v70
	v_fmac_f32_e32 v20, v38, v78
	v_fmac_f32_e32 v21, v38, v88
	v_fmac_f32_e32 v18, v39, v63
	v_fmac_f32_e32 v19, v39, v71
	v_fmac_f32_e32 v20, v39, v79
	v_fmac_f32_e32 v21, v39, v89
	v_fmac_f32_e32 v18, v40, v64
	v_fmac_f32_e32 v19, v40, v72
	v_fmac_f32_e32 v20, v40, v80
	v_fmac_f32_e32 v21, v40, v90
	v_fmac_f32_e32 v18, v41, v65
	v_fmac_f32_e32 v19, v41, v73
	v_fmac_f32_e32 v20, v41, v81
	v_fmac_f32_e32 v21, v41, v91
	ds_read_b128 v[58:61], v25
	ds_read_b128 v[62:65], v25 offset:16
	ds_read_b128 v[66:69], v25 offset:2048
	ds_read_b128 v[70:73], v25 offset:2064
	ds_read_b128 v[74:77], v25 offset:4096
	ds_read_b128 v[78:81], v25 offset:4112
	ds_read_b128 v[84:87], v25 offset:6144
	ds_read_b128 v[88:91], v25 offset:6160
	v_add_u32_e32 v25, 32, v25
	s_waitcnt vmcnt(8)
	s_waitcnt lgkmcnt(0)
	v_fmac_f32_e32 v18, v42, v58
	v_fmac_f32_e32 v19, v42, v66
	v_fmac_f32_e32 v20, v42, v74
	v_fmac_f32_e32 v21, v42, v84
	v_fmac_f32_e32 v18, v43, v59
	v_fmac_f32_e32 v19, v43, v67
	v_fmac_f32_e32 v20, v43, v75
	v_fmac_f32_e32 v21, v43, v85
	v_fmac_f32_e32 v18, v44, v60
	v_fmac_f32_e32 v19, v44, v68
	v_fmac_f32_e32 v20, v44, v76
	v_fmac_f32_e32 v21, v44, v86
	v_fmac_f32_e32 v18, v45, v61
	v_fmac_f32_e32 v19, v45, v69
	v_fmac_f32_e32 v20, v45, v77
	v_fmac_f32_e32 v21, v45, v87
	v_fmac_f32_e32 v18, v46, v62
	v_fmac_f32_e32 v19, v46, v70
	v_fmac_f32_e32 v20, v46, v78
	v_fmac_f32_e32 v21, v46, v88
	v_fmac_f32_e32 v18, v47, v63
	v_fmac_f32_e32 v19, v47, v71
	v_fmac_f32_e32 v20, v47, v79
	v_fmac_f32_e32 v21, v47, v89
	v_fmac_f32_e32 v18, v48, v64
	v_fmac_f32_e32 v19, v48, v72
	v_fmac_f32_e32 v20, v48, v80
	v_fmac_f32_e32 v21, v48, v90
	v_fmac_f32_e32 v18, v49, v65
	v_fmac_f32_e32 v19, v49, v73
	v_fmac_f32_e32 v20, v49, v81
	v_fmac_f32_e32 v21, v49, v91
	ds_read_b128 v[58:61], v25
	ds_read_b128 v[62:65], v25 offset:16
	ds_read_b128 v[66:69], v25 offset:2048
	ds_read_b128 v[70:73], v25 offset:2064
	ds_read_b128 v[74:77], v25 offset:4096
	ds_read_b128 v[78:81], v25 offset:4112
	ds_read_b128 v[84:87], v25 offset:6144
	ds_read_b128 v[88:91], v25 offset:6160
	v_add_u32_e32 v25, 32, v25
	s_waitcnt vmcnt(0)
	s_waitcnt lgkmcnt(0)
	v_fmac_f32_e32 v18, v50, v58
	v_fmac_f32_e32 v19, v50, v66
	v_fmac_f32_e32 v20, v50, v74
	v_fmac_f32_e32 v21, v50, v84
	v_fmac_f32_e32 v18, v51, v59
	v_fmac_f32_e32 v19, v51, v67
	v_fmac_f32_e32 v20, v51, v75
	v_fmac_f32_e32 v21, v51, v85
	v_fmac_f32_e32 v18, v52, v60
	v_fmac_f32_e32 v19, v52, v68
	v_fmac_f32_e32 v20, v52, v76
	v_fmac_f32_e32 v21, v52, v86
	v_fmac_f32_e32 v18, v53, v61
	v_fmac_f32_e32 v19, v53, v69
	v_fmac_f32_e32 v20, v53, v77
	v_fmac_f32_e32 v21, v53, v87
	v_fmac_f32_e32 v18, v54, v62
	v_fmac_f32_e32 v19, v54, v70
	v_fmac_f32_e32 v20, v54, v78
	v_fmac_f32_e32 v21, v54, v88
	v_fmac_f32_e32 v18, v55, v63
	v_fmac_f32_e32 v19, v55, v71
	v_fmac_f32_e32 v20, v55, v79
	v_fmac_f32_e32 v21, v55, v89
	v_fmac_f32_e32 v18, v56, v64
	v_fmac_f32_e32 v19, v56, v72
	v_fmac_f32_e32 v20, v56, v80
	v_fmac_f32_e32 v21, v56, v90
	v_fmac_f32_e32 v18, v57, v65
	v_fmac_f32_e32 v19, v57, v73
	v_fmac_f32_e32 v20, v57, v81
	v_fmac_f32_e32 v21, v57, v91
	v_lshlrev_b32_e32 v0, 2, v24
	v_lshl_or_b32 v1, v3, 11, v0
	ds_write2st64_b32 v1, v18, v19 offset0:32 offset1:34
	ds_write2st64_b32 v1, v20, v21 offset0:36 offset1:38
	v_lshl_or_b32 v1, v3, 10, v0
	s_waitcnt lgkmcnt(0)
	s_barrier
	ds_read2st64_b32 v[6:7], v1 offset0:32 offset1:40
	v_mov_b32_e32 v4, s6
	v_mov_b32_e32 v5, s7
	v_lshl_add_u32 v0, v3, 1, s16
	v_ashrrev_i32_e32 v3, 31, v2
	v_lshl_add_u64 v[4:5], v[2:3], 2, v[4:5]
	s_waitcnt lgkmcnt(0)
	v_add_f32_e32 v3, v6, v7
	v_cmp_lt_i32_e64 s[2:3], 63, v0
	s_and_saveexec_b64 s[6:7], s[2:3]
	s_xor_b64 s[6:7], exec, s[6:7]
	s_cbranch_execz .LBB0_145
	s_movk_i32 s2, 0x41
	v_cmp_lt_i32_e64 s[2:3], s2, v0
	s_and_saveexec_b64 s[8:9], s[2:3]
	s_xor_b64 s[8:9], exec, s[8:9]
	s_cbranch_execz .LBB0_140
	s_movk_i32 s2, 0x42
	v_cmp_eq_u32_e64 s[2:3], s2, v0
	s_and_saveexec_b64 s[10:11], s[2:3]
	s_cbranch_execz .LBB0_139
	v_readlane_b32 s12, v83, 0
	v_readlane_b32 s14, v83, 2
	v_readlane_b32 s16, v83, 4
	v_readlane_b32 s15, v83, 3
	v_readlane_b32 s17, v83, 5
	v_mov_b32_e32 v7, s16
	v_mov_b32_e32 v8, s14
	v_readlane_b32 s13, v83, 1
	v_cndmask_b32_e32 v7, v7, v8, vcc
	v_mov_b32_e32 v8, s17
	v_mov_b32_e32 v9, s15
	v_cndmask_b32_e32 v8, v8, v9, vcc
	v_mov_b32_e32 v9, s13
	v_or_b32_e32 v6, v23, v22
	v_cndmask_b32_e64 v9, v8, v9, s[0:1]
	v_mov_b32_e32 v8, s12
	v_cndmask_b32_e64 v8, v7, v8, s[0:1]
	v_ashrrev_i32_e32 v7, 31, v6
	v_lshl_add_u64 v[6:7], v[6:7], 2, v[8:9]
	global_load_dword v7, v[6:7], off
	v_add_co_u32_e32 v6, vcc, 0x3000, v4
	v_readlane_b32 s18, v83, 6
	v_readlane_b32 s19, v83, 7
	v_readlane_b32 s20, v83, 8
	v_readlane_b32 s21, v83, 9
	v_readlane_b32 s22, v83, 10
	v_readlane_b32 s23, v83, 11
	v_readlane_b32 s24, v83, 12
	v_readlane_b32 s25, v83, 13
	v_readlane_b32 s26, v83, 14
	v_readlane_b32 s27, v83, 15
	s_waitcnt vmcnt(0)
	v_add_f32_e32 v3, v3, v7
	v_addc_co_u32_e32 v7, vcc, 0, v5, vcc
	global_store_dword v[6:7], v3, off

	.amdhsa_kernel _Z13stage0_kernel5TJobs6S0Args
		.amdhsa_group_segment_fixed_size 16640
		.amdhsa_private_segment_fixed_size 0
		.amdhsa_kernarg_size 568
		.amdhsa_user_sgpr_count 2
		.amdhsa_user_sgpr_dispatch_ptr 0
		.amdhsa_user_sgpr_queue_ptr 0
		.amdhsa_user_sgpr_kernarg_segment_ptr 1
		.amdhsa_user_sgpr_dispatch_id 0
		.amdhsa_user_sgpr_kernarg_preload_length 0
		.amdhsa_user_sgpr_kernarg_preload_offset 0
		.amdhsa_user_sgpr_private_segment_size 0
		.amdhsa_uses_dynamic_stack 0
		.amdhsa_enable_private_segment 0
		.amdhsa_system_sgpr_workgroup_id_x 1
		.amdhsa_system_sgpr_workgroup_id_y 0
		.amdhsa_system_sgpr_workgroup_id_z 0
		.amdhsa_system_sgpr_workgroup_info 0
		.amdhsa_system_vgpr_workitem_id 0
		.amdhsa_next_free_vgpr 96
		.amdhsa_next_free_sgpr 100
		.amdhsa_accum_offset 96
		.amdhsa_reserve_vcc 1
		.amdhsa_float_round_mode_32 0
		.amdhsa_float_round_mode_16_64 0
		.amdhsa_float_denorm_mode_32 3
		.amdhsa_float_denorm_mode_16_64 3
		.amdhsa_dx10_clamp 1
		.amdhsa_ieee_mode 1
		.amdhsa_fp16_overflow 0
		.amdhsa_tg_split 0
		.amdhsa_exception_fp_ieee_invalid_op 0
		.amdhsa_exception_fp_denorm_src 0
		.amdhsa_exception_fp_ieee_div_zero 0
		.amdhsa_exception_fp_ieee_overflow 0
		.amdhsa_exception_fp_ieee_underflow 0
		.amdhsa_exception_fp_ieee_inexact 0
		.amdhsa_exception_int_div_zero 0
	.end_amdhsa_kernel

.LBB4_47:
	s_endpgm
	.p2align	8

.LBB5_7:
	s_load_dwordx2 s[2:3], s[0:1], 0x38
	v_lshrrev_b32_e32 v1, 1, v0
	v_bfe_u32 v138, v0, 5, 1
	v_and_b32_e32 v142, 0xc0, v1
	v_lshlrev_b32_e32 v1, 7, v139
	v_and_b32_e32 v140, 31, v0
	v_and_b32_e32 v141, 0x80, v1
	v_or_b32_e32 v1, 2, v138
	s_and_b64 vcc, exec, s[14:15]
	s_cbranch_vccz .LBB5_20
	v_or_b32_e32 v2, v142, v140
	v_bitop3_b32 v4, v1, v11, 3 bitop3:0x78
	v_lshlrev_b32_e32 v144, 6, v2
	v_lshlrev_b32_e32 v146, 4, v4
	v_or_b32_e32 v2, v141, v140
	v_add_u32_e32 v4, s16, v11
	v_lshlrev_b32_e32 v147, 6, v2
	v_min_i32_e32 v2, s24, v4
	v_mul_lo_u32 v2, s6, v2
	v_bitop3_b32 v3, v138, v11, 3 bitop3:0x78
	v_add3_u32 v2, v2, s9, v10
	v_lshlrev_b32_e32 v145, 4, v3
	v_ashrrev_i32_e32 v3, 31, v2
	v_lshl_add_u64 v[2:3], v[2:3], 1, s[4:5]
	s_mov_b64 s[26:27], 0xc0
	v_lshl_add_u64 v[130:131], v[2:3], 0, s[26:27]
	v_add_u32_e32 v2, 0x80, v4
	v_min_i32_e32 v2, s24, v2
	v_mul_lo_u32 v2, s6, v2
	v_add3_u32 v2, v2, s9, v10
	v_ashrrev_i32_e32 v3, 31, v2
	s_mul_i32 s19, s19, s21
	v_lshl_add_u64 v[2:3], v[2:3], 1, s[4:5]
	s_sub_i32 s4, s22, s19
	s_sub_i32 s4, s4, s23
	s_mul_i32 s4, s10, s4
	s_lshl_b32 s4, s4, 8
	s_lshl_b32 s5, s20, 8
	s_add_i32 s5, s5, s4
	v_or_b32_e32 v4, s5, v11
	v_lshl_add_u64 v[132:133], v[2:3], 0, s[26:27]
	v_mul_lo_u32 v2, s8, v4
	v_add3_u32 v2, v2, s9, v10
	v_ashrrev_i32_e32 v3, 31, v2
	v_lshl_add_u64 v[2:3], v[2:3], 1, s[12:13]
	v_lshl_add_u64 v[134:135], v[2:3], 0, s[26:27]
	v_or_b32_e32 v2, 0x80, v4
	v_mul_lo_u32 v2, s8, v2
	v_add3_u32 v2, v2, s9, v10
	v_ashrrev_i32_e32 v3, 31, v2
	v_lshl_add_u64 v[2:3], v[2:3], 1, s[12:13]
	v_lshl_add_u64 v[136:137], v[2:3], 0, s[26:27]
	v_mov_b32_e32 v2, 0
	s_mov_b32 s14, 3
	s_add_i32 s15, s18, -1
	s_mov_b32 s6, 0
	s_mov_b64 s[4:5], 0
	s_mov_b32 s10, 3
	v_mov_b32_e32 v3, v2
	v_mov_b32_e32 v4, v2
	v_mov_b32_e32 v5, v2
	v_mov_b32_e32 v6, v2
	v_mov_b32_e32 v7, v2
	v_mov_b32_e32 v8, v2
	v_mov_b32_e32 v9, v2
	v_mov_b32_e32 v10, v2
	v_mov_b32_e32 v11, v2
	v_mov_b32_e32 v12, v2
	v_mov_b32_e32 v13, v2
	v_mov_b32_e32 v14, v2
	v_mov_b32_e32 v15, v2
	v_mov_b32_e32 v16, v2
	v_mov_b32_e32 v17, v2
	v_mov_b32_e32 v18, v2
	v_mov_b32_e32 v19, v2
	v_mov_b32_e32 v20, v2
	v_mov_b32_e32 v21, v2
	v_mov_b32_e32 v22, v2
	v_mov_b32_e32 v23, v2
	v_mov_b32_e32 v24, v2
	v_mov_b32_e32 v25, v2
	v_mov_b32_e32 v26, v2
	v_mov_b32_e32 v27, v2
	v_mov_b32_e32 v28, v2
	v_mov_b32_e32 v29, v2
	v_mov_b32_e32 v30, v2
	v_mov_b32_e32 v31, v2
	v_mov_b32_e32 v32, v2
	v_mov_b32_e32 v33, v2
	v_mov_b32_e32 v34, v2
	v_mov_b32_e32 v35, v2
	v_mov_b32_e32 v36, v2
	v_mov_b32_e32 v37, v2
	v_mov_b32_e32 v38, v2
	v_mov_b32_e32 v39, v2
	v_mov_b32_e32 v40, v2
	v_mov_b32_e32 v41, v2
	v_mov_b32_e32 v42, v2
	v_mov_b32_e32 v43, v2
	v_mov_b32_e32 v44, v2
	v_mov_b32_e32 v45, v2
	v_mov_b32_e32 v46, v2
	v_mov_b32_e32 v47, v2
	v_mov_b32_e32 v48, v2
	v_mov_b32_e32 v49, v2
	v_mov_b32_e32 v50, v2
	v_mov_b32_e32 v51, v2
	v_mov_b32_e32 v52, v2
	v_mov_b32_e32 v53, v2
	v_mov_b32_e32 v54, v2
	v_mov_b32_e32 v55, v2
	v_mov_b32_e32 v56, v2
	v_mov_b32_e32 v57, v2
	v_mov_b32_e32 v58, v2
	v_mov_b32_e32 v59, v2
	v_mov_b32_e32 v60, v2
	v_mov_b32_e32 v61, v2
	v_mov_b32_e32 v62, v2
	v_mov_b32_e32 v63, v2
	v_mov_b32_e32 v64, v2
	v_mov_b32_e32 v65, v2
	v_mov_b32_e32 v66, v2
	v_mov_b32_e32 v67, v2
	v_mov_b32_e32 v68, v2
	v_mov_b32_e32 v69, v2
	v_mov_b32_e32 v70, v2
	v_mov_b32_e32 v71, v2
	v_mov_b32_e32 v72, v2
	v_mov_b32_e32 v73, v2
	v_mov_b32_e32 v74, v2
	v_mov_b32_e32 v75, v2
	v_mov_b32_e32 v76, v2
	v_mov_b32_e32 v77, v2
	v_mov_b32_e32 v78, v2
	v_mov_b32_e32 v79, v2
	v_mov_b32_e32 v80, v2
	v_mov_b32_e32 v81, v2
	v_mov_b32_e32 v82, v2
	v_mov_b32_e32 v83, v2
	v_mov_b32_e32 v84, v2
	v_mov_b32_e32 v85, v2
	v_mov_b32_e32 v86, v2
	v_mov_b32_e32 v87, v2
	v_mov_b32_e32 v88, v2
	v_mov_b32_e32 v89, v2
	v_mov_b32_e32 v90, v2
	v_mov_b32_e32 v91, v2
	v_mov_b32_e32 v92, v2
	v_mov_b32_e32 v93, v2
	v_mov_b32_e32 v94, v2
	v_mov_b32_e32 v95, v2
	v_mov_b32_e32 v96, v2
	v_mov_b32_e32 v97, v2
	v_mov_b32_e32 v98, v2
	v_mov_b32_e32 v99, v2
	v_mov_b32_e32 v100, v2
	v_mov_b32_e32 v101, v2
	v_mov_b32_e32 v102, v2
	v_mov_b32_e32 v103, v2
	v_mov_b32_e32 v104, v2
	v_mov_b32_e32 v105, v2
	v_mov_b32_e32 v106, v2
	v_mov_b32_e32 v107, v2
	v_mov_b32_e32 v108, v2
	v_mov_b32_e32 v109, v2
	v_mov_b32_e32 v110, v2
	v_mov_b32_e32 v111, v2
	v_mov_b32_e32 v112, v2
	v_mov_b32_e32 v113, v2
	v_mov_b32_e32 v114, v2
	v_mov_b32_e32 v115, v2
	v_mov_b32_e32 v116, v2
	v_mov_b32_e32 v117, v2
	v_mov_b32_e32 v118, v2
	v_mov_b32_e32 v119, v2
	v_mov_b32_e32 v120, v2
	v_mov_b32_e32 v121, v2
	v_mov_b32_e32 v122, v2
	v_mov_b32_e32 v123, v2
	v_mov_b32_e32 v124, v2
	v_mov_b32_e32 v125, v2
	v_mov_b32_e32 v126, v2
	v_mov_b32_e32 v127, v2
	v_mov_b32_e32 v128, v2
	v_mov_b32_e32 v129, v2
	v_readfirstlane_b32 s28, v143
	v_add_u32_e32 v172, v144, v145
	v_add_u32_e32 v173, v144, v146
	v_add_u32_e32 v144, v147, v145
	v_add_u32_e32 v147, v147, v146
	v_mov_b32_e32 v145, v172
	v_mov_b32_e32 v146, v173
	s_mov_b32 s9, 0x18000
	s_or_b32 m0, s9, s28
	s_nop 0
	global_load_lds_dwordx4 v[130:131], off
	v_lshl_add_u64 v[130:131], v[130:131], 0, 64
	s_add_u32 m0, m0, 0x2000
	global_load_lds_dwordx4 v[132:133], off
	v_lshl_add_u64 v[132:133], v[132:133], 0, 64
	s_add_u32 m0, m0, 0x2000
	global_load_lds_dwordx4 v[134:135], off
	v_lshl_add_u64 v[134:135], v[134:135], 0, 64
	s_add_u32 m0, m0, 0x2000
	global_load_lds_dwordx4 v[136:137], off
	v_lshl_add_u64 v[136:137], v[136:137], 0, 64
	s_mov_b32 s10, 4
	s_waitcnt vmcnt(12)
	s_barrier
	ds_read_b128 v[148:151], v145
	ds_read_b128 v[152:155], v144 offset:16384
	ds_read_b128 v[160:163], v144 offset:18432
	ds_read_b128 v[156:159], v145 offset:2048
	ds_read_b128 v[164:167], v144 offset:20480
	ds_read_b128 v[168:171], v144 offset:22528
.Lk5_loop:
	s_waitcnt vmcnt(8)
	s_waitcnt lgkmcnt(0)
	s_barrier
	s_lshl_b32 s8, s6, 15
	v_add_u32_e32 v172, s8, v146
	v_add_u32_e32 v173, s8, v147
	ds_read_b128 v[176:179], v172
	ds_read_b128 v[184:187], v173 offset:16384
	ds_read_b128 v[188:191], v173 offset:18432
	ds_read_b128 v[180:183], v172 offset:2048
	ds_read_b128 v[192:195], v173 offset:20480
	ds_read_b128 v[196:199], v173 offset:22528
	s_lshl_b32 s9, s10, 15
	s_or_b32 m0, s9, s28
	v_mfma_f32_32x32x16_f16 v[114:129], v[148:151], v[152:155], v[114:129]
	global_load_lds_dwordx4 v[130:131], off
	v_lshl_add_u64 v[130:131], v[130:131], 0, 64
	s_add_u32 m0, m0, 0x2000
	v_mfma_f32_32x32x16_f16 v[98:113], v[148:151], v[160:163], v[98:113]
	global_load_lds_dwordx4 v[132:133], off
	v_lshl_add_u64 v[132:133], v[132:133], 0, 64
	s_add_u32 m0, m0, 0x2000
	v_mfma_f32_32x32x16_f16 v[82:97], v[148:151], v[164:167], v[82:97]
	global_load_lds_dwordx4 v[134:135], off
	v_lshl_add_u64 v[134:135], v[134:135], 0, 64
	s_add_u32 m0, m0, 0x2000
	v_mfma_f32_32x32x16_f16 v[66:81], v[148:151], v[168:171], v[66:81]
	global_load_lds_dwordx4 v[136:137], off
	v_lshl_add_u64 v[136:137], v[136:137], 0, 64
	v_mfma_f32_32x32x16_f16 v[50:65], v[156:159], v[152:155], v[50:65]
	s_add_i32 s6, s6, 1
	s_cmp_eq_u32 s6, 5
	s_cselect_b32 s6, 0, s6
	s_lshl_b32 s8, s6, 15
	v_mfma_f32_32x32x16_f16 v[34:49], v[156:159], v[160:163], v[34:49]
	v_add_u32_e32 v172, s8, v145
	v_add_u32_e32 v173, s8, v144
	v_mfma_f32_32x32x16_f16 v[18:33], v[156:159], v[164:167], v[18:33]
	s_add_i32 s10, s10, 1
	s_cmp_eq_u32 s10, 5
	s_cselect_b32 s10, 0, s10
	v_mfma_f32_32x32x16_f16 v[2:17], v[156:159], v[168:171], v[2:17]
	s_waitcnt lgkmcnt(0)
	v_mfma_f32_32x32x16_f16 v[114:129], v[176:179], v[184:187], v[114:129]
	ds_read_b128 v[148:151], v172
	ds_read_b128 v[152:155], v173 offset:16384
	v_mfma_f32_32x32x16_f16 v[98:113], v[176:179], v[188:191], v[98:113]
	ds_read_b128 v[160:163], v173 offset:18432
	ds_read_b128 v[156:159], v172 offset:2048
	v_mfma_f32_32x32x16_f16 v[82:97], v[176:179], v[192:195], v[82:97]
	ds_read_b128 v[164:167], v173 offset:20480
	ds_read_b128 v[168:171], v173 offset:22528
	v_mfma_f32_32x32x16_f16 v[66:81], v[176:179], v[196:199], v[66:81]
	v_mfma_f32_32x32x16_f16 v[50:65], v[180:183], v[184:187], v[50:65]
	s_add_i32 s15, s15, -1
	s_cmp_lg_u32 s15, -1
	v_mfma_f32_32x32x16_f16 v[34:49], v[180:183], v[188:191], v[34:49]
	v_mfma_f32_32x32x16_f16 v[18:33], v[180:183], v[192:195], v[18:33]
	v_mfma_f32_32x32x16_f16 v[2:17], v[180:183], v[196:199], v[2:17]
	s_cbranch_scc1 .Lk5_loop
	s_branch .LBB5_21

	.amdhsa_kernel _Z11gemm_kernelILi4ELi2ELi2ELi4ELi4ELi3ELi2ELb0EEvPKDF16_iiS1_iiiiiPKfPfPDF16_i
		.amdhsa_group_segment_fixed_size 163840
		.amdhsa_private_segment_fixed_size 0
		.amdhsa_kernarg_size 76
		.amdhsa_user_sgpr_count 2
		.amdhsa_user_sgpr_dispatch_ptr 0
		.amdhsa_user_sgpr_queue_ptr 0
		.amdhsa_user_sgpr_kernarg_segment_ptr 1
		.amdhsa_user_sgpr_dispatch_id 0
		.amdhsa_user_sgpr_kernarg_preload_length 0
		.amdhsa_user_sgpr_kernarg_preload_offset 0
		.amdhsa_user_sgpr_private_segment_size 0
		.amdhsa_uses_dynamic_stack 0
		.amdhsa_enable_private_segment 0
		.amdhsa_system_sgpr_workgroup_id_x 1
		.amdhsa_system_sgpr_workgroup_id_y 0
		.amdhsa_system_sgpr_workgroup_id_z 0
		.amdhsa_system_sgpr_workgroup_info 0
		.amdhsa_system_vgpr_workitem_id 0
		.amdhsa_next_free_vgpr 200
		.amdhsa_next_free_sgpr 96
		.amdhsa_accum_offset 200
		.amdhsa_reserve_vcc 1
		.amdhsa_float_round_mode_32 0
		.amdhsa_float_round_mode_16_64 0
		.amdhsa_float_denorm_mode_32 3
		.amdhsa_float_denorm_mode_16_64 3
		.amdhsa_dx10_clamp 1
		.amdhsa_ieee_mode 1
		.amdhsa_fp16_overflow 0
		.amdhsa_tg_split 0
		.amdhsa_exception_fp_ieee_invalid_op 0
		.amdhsa_exception_fp_denorm_src 0
		.amdhsa_exception_fp_ieee_div_zero 0
		.amdhsa_exception_fp_ieee_overflow 0
		.amdhsa_exception_fp_ieee_underflow 0
		.amdhsa_exception_fp_ieee_inexact 0
		.amdhsa_exception_int_div_zero 0
	.end_amdhsa_kernel

	.text
	.p2alignl 6, 3212836864
	.fill 256, 4, 3212836864
	.p2align	8

amdhsa.kernels:
  - .agpr_count:     0
    .args:
      - .offset:         0
        .size:           288
        .value_kind:     by_value
      - .offset:         288
        .size:           280
        .value_kind:     by_value
    .group_segment_fixed_size: 16640
    .kernarg_segment_align: 8
    .kernarg_segment_size: 568
    .language:       OpenCL C
    .language_version:
      - 2
      - 0
    .max_flat_workgroup_size: 256
    .name:           _Z13stage0_kernel5TJobs6S0Args
    .private_segment_fixed_size: 0
    .sgpr_count:     106
    .sgpr_spill_count: 213
    .symbol:         _Z13stage0_kernel5TJobs6S0Args.kd
    .uniform_work_group_size: 1
    .uses_dynamic_stack: false
    .vgpr_count:     96
    .vgpr_spill_count: 0
    .wavefront_size: 64
  - .agpr_count:     0
    .args:
      - .actual_access:  read_only
        .address_space:  global
        .offset:         0
        .size:           8
        .value_kind:     global_buffer
      - .actual_access:  read_only
        .address_space:  global
        .offset:         8
        .size:           8
        .value_kind:     global_buffer
      - .actual_access:  write_only
        .address_space:  global
        .offset:         16
        .size:           8
        .value_kind:     global_buffer
      - .offset:         24
        .size:           4
        .value_kind:     by_value
      - .offset:         28
        .size:           4
        .value_kind:     by_value
    .group_segment_fixed_size: 0
    .kernarg_segment_align: 8
    .kernarg_segment_size: 32
    .language:       OpenCL C
    .language_version:
      - 2
      - 0
    .max_flat_workgroup_size: 256
    .name:           _Z11gelu_reducePKfS0_PDF16_ii
    .private_segment_fixed_size: 0
    .sgpr_count:     18
    .sgpr_spill_count: 0
    .symbol:         _Z11gelu_reducePKfS0_PDF16_ii.kd
    .uniform_work_group_size: 1
    .uses_dynamic_stack: false
    .vgpr_count:     17
    .vgpr_spill_count: 0
    .wavefront_size: 64
  - .agpr_count:     0
    .args:
      - .address_space:  global
        .offset:         0
        .size:           8
        .value_kind:     global_buffer
      - .address_space:  global
        .offset:         8
        .size:           8
        .value_kind:     global_buffer
      - .actual_access:  read_only
        .address_space:  global
        .offset:         16
        .size:           8
        .value_kind:     global_buffer
      - .actual_access:  write_only
        .address_space:  global
        .offset:         24
        .size:           8
        .value_kind:     global_buffer
    .group_segment_fixed_size: 75776
    .kernarg_segment_align: 8
    .kernarg_segment_size: 32
    .language:       OpenCL C
    .language_version:
      - 2
      - 0
    .max_flat_workgroup_size: 512
    .name:           _Z11front_statsPKDF16_S0_PKfPf
    .private_segment_fixed_size: 0
    .sgpr_count:     18
    .sgpr_spill_count: 0
    .symbol:         _Z11front_statsPKDF16_S0_PKfPf.kd
    .uniform_work_group_size: 1
    .uses_dynamic_stack: false
    .vgpr_count:     86
    .vgpr_spill_count: 0
    .wavefront_size: 64
  - .agpr_count:     0
    .args:
      - .actual_access:  read_only
        .address_space:  global
        .offset:         0
        .size:           8
        .value_kind:     global_buffer
      - .actual_access:  read_only
        .address_space:  global
        .offset:         8
        .size:           8
        .value_kind:     global_buffer
      - .actual_access:  read_only
        .address_space:  global
        .offset:         16
        .size:           8
        .value_kind:     global_buffer
      - .actual_access:  read_only
        .address_space:  global
        .offset:         24
        .size:           8
        .value_kind:     global_buffer
      - .actual_access:  read_only
        .address_space:  global
        .offset:         32
        .size:           8
        .value_kind:     global_buffer
      - .actual_access:  read_only
        .address_space:  global
        .offset:         40
        .size:           8
        .value_kind:     global_buffer
      - .actual_access:  read_only
        .address_space:  global
        .offset:         48
        .size:           8
        .value_kind:     global_buffer
      - .actual_access:  write_only
        .address_space:  global
        .offset:         56
        .size:           8
        .value_kind:     global_buffer
    .group_segment_fixed_size: 49152
    .kernarg_segment_align: 8
    .kernarg_segment_size: 64
    .language:       OpenCL C
    .language_version:
      - 2
      - 0
    .max_flat_workgroup_size: 256
    .name:           _Z12attn2_kernelPKDF16_S0_PKfS2_S2_PKiS2_PDF16_
    .private_segment_fixed_size: 0
    .sgpr_count:     82
    .sgpr_spill_count: 0
    .symbol:         _Z12attn2_kernelPKDF16_S0_PKfS2_S2_PKiS2_PDF16_.kd
    .uniform_work_group_size: 1
    .uses_dynamic_stack: false
    .vgpr_count:     166
    .vgpr_spill_count: 0
    .wavefront_size: 64
  - .agpr_count:     0
    .args:
      - .address_space:  global
        .offset:         0
        .size:           8
        .value_kind:     global_buffer
      - .offset:         8
        .size:           4
        .value_kind:     by_value
      - .offset:         12
        .size:           4
        .value_kind:     by_value
      - .address_space:  global
        .offset:         16
        .size:           8
        .value_kind:     global_buffer
      - .offset:         24
        .size:           4
        .value_kind:     by_value
      - .offset:         28
        .size:           4
        .value_kind:     by_value
      - .offset:         32
        .size:           4
        .value_kind:     by_value
      - .offset:         36
        .size:           4
        .value_kind:     by_value
      - .offset:         40
        .size:           4
        .value_kind:     by_value
      - .actual_access:  read_only
        .address_space:  global
        .offset:         48
        .size:           8
        .value_kind:     global_buffer
      - .actual_access:  write_only
        .address_space:  global
        .offset:         56
        .size:           8
        .value_kind:     global_buffer
      - .actual_access:  write_only
        .address_space:  global
        .offset:         64
        .size:           8
        .value_kind:     global_buffer
      - .offset:         72
        .size:           4
        .value_kind:     by_value
    .group_segment_fixed_size: 73728
    .kernarg_segment_align: 8
    .kernarg_segment_size: 76
    .language:       OpenCL C
    .language_version:
      - 2
      - 0
    .max_flat_workgroup_size: 512
    .name:           _Z11gemm_kernelILi2ELi4ELi2ELi2ELi3ELi0ELi4ELb0EEvPKDF16_iiS1_iiiiiPKfPfPDF16_i
    .private_segment_fixed_size: 0
    .sgpr_count:     33
    .sgpr_spill_count: 0
    .symbol:         _Z11gemm_kernelILi2ELi4ELi2ELi2ELi3ELi0ELi4ELb0EEvPKDF16_iiS1_iiiiiPKfPfPDF16_i.kd
    .uniform_work_group_size: 1
    .uses_dynamic_stack: false
    .vgpr_count:     96
    .vgpr_spill_count: 0
    .wavefront_size: 64
  - .agpr_count:     0
    .args:
      - .address_space:  global
        .offset:         0
        .size:           8
        .value_kind:     global_buffer
      - .offset:         8
        .size:           4
        .value_kind:     by_value
      - .offset:         12
        .size:           4
        .value_kind:     by_value
      - .address_space:  global
        .offset:         16
        .size:           8
        .value_kind:     global_buffer
      - .offset:         24
        .size:           4
        .value_kind:     by_value
      - .offset:         28
        .size:           4
        .value_kind:     by_value
      - .offset:         32
        .size:           4
        .value_kind:     by_value
      - .offset:         36
        .size:           4
        .value_kind:     by_value
      - .offset:         40
        .size:           4
        .value_kind:     by_value
      - .actual_access:  read_only
        .address_space:  global
        .offset:         48
        .size:           8
        .value_kind:     global_buffer
      - .actual_access:  write_only
        .address_space:  global
        .offset:         56
        .size:           8
        .value_kind:     global_buffer
      - .actual_access:  read_only
        .address_space:  global
        .offset:         64
        .size:           8
        .value_kind:     global_buffer
      - .offset:         72
        .size:           4
        .value_kind:     by_value
    .group_segment_fixed_size: 163840
    .kernarg_segment_align: 8
    .kernarg_segment_size: 76
    .language:       OpenCL C
    .language_version:
      - 2
      - 0
    .max_flat_workgroup_size: 512
    .name:           _Z11gemm_kernelILi4ELi2ELi2ELi4ELi4ELi3ELi2ELb0EEvPKDF16_iiS1_iiiiiPKfPfPDF16_i
    .private_segment_fixed_size: 0
    .sgpr_count:     35
    .sgpr_spill_count: 0
    .symbol:         _Z11gemm_kernelILi4ELi2ELi2ELi4ELi4ELi3ELi2ELb0EEvPKDF16_iiS1_iiiiiPKfPfPDF16_i.kd
    .uniform_work_group_size: 1
    .uses_dynamic_stack: false
    .vgpr_count:     200
    .vgpr_spill_count: 0
    .wavefront_size: 64
  - .agpr_count:     0
    .args:
      - .address_space:  global
        .offset:         0
        .size:           8
        .value_kind:     global_buffer
      - .offset:         8
        .size:           4
        .value_kind:     by_value
      - .offset:         12
        .size:           4
        .value_kind:     by_value
      - .address_space:  global
        .offset:         16
        .size:           8
        .value_kind:     global_buffer
      - .offset:         24
        .size:           4
        .value_kind:     by_value
      - .offset:         28
        .size:           4
        .value_kind:     by_value
      - .offset:         32
        .size:           4
        .value_kind:     by_value
      - .offset:         36
        .size:           4
        .value_kind:     by_value
      - .offset:         40
        .size:           4
        .value_kind:     by_value
      - .actual_access:  read_only
        .address_space:  global
        .offset:         48
        .size:           8
        .value_kind:     global_buffer
      - .actual_access:  write_only
        .address_space:  global
        .offset:         56
        .size:           8
        .value_kind:     global_buffer
      - .actual_access:  read_only
        .address_space:  global
        .offset:         64
        .size:           8
        .value_kind:     global_buffer
      - .offset:         72
        .size:           4
        .value_kind:     by_value
    .group_segment_fixed_size: 65536
    .kernarg_segment_align: 8
    .kernarg_segment_size: 76
    .language:       OpenCL C
    .language_version:
      - 2
      - 0
    .max_flat_workgroup_size: 512
    .name:           _Z11gemm_kernelILi2ELi4ELi2ELi1ELi4ELi2ELi2ELb0EEvPKDF16_iiS1_iiiiiPKfPfPDF16_i
    .private_segment_fixed_size: 0
    .sgpr_count:     26
    .sgpr_spill_count: 0
    .symbol:         _Z11gemm_kernelILi2ELi4ELi2ELi1ELi4ELi2ELi2ELb0EEvPKDF16_iiS1_iiiiiPKfPfPDF16_i.kd
    .uniform_work_group_size: 1
    .uses_dynamic_stack: false
    .vgpr_count:     64
    .vgpr_spill_count: 0
    .wavefront_size: 64
